# P10 next-norm/modulate: gain/scale/shift loads hoisted into free VGPR quads (19 in flight)
# baseline (speedup 1.0000x reference)
.LBB0_2493:
	v_mov_b32_e32 v4, s66
	ds_read_b64 v[4:5], v4
	v_mov_b32_e32 v6, v65
	v_mov_b32_e32 v7, v57
	v_mov_b32_e32 v82, v67
	v_mov_b32_e32 v83, v59
	s_waitcnt lgkmcnt(0)
	v_readfirstlane_b32 s2, v4
	v_readfirstlane_b32 s3, v5
	v_mov_b32_e32 v4, v64
	v_mov_b32_e32 v5, v56
	v_pk_mul_f32 v[6:7], v[6:7], v[6:7]
	v_mov_b32_e32 v80, v66
	v_mov_b32_e32 v81, v58
	v_pk_mul_f32 v[82:83], v[82:83], v[82:83]
	v_pk_fma_f32 v[4:5], v[4:5], v[4:5], v[6:7]
	v_pk_fma_f32 v[6:7], v[80:81], v[80:81], v[82:83]
	v_mov_b32_e32 v80, v142
	v_pk_add_f32 v[4:5], v[4:5], v[6:7]
	v_pk_mul_f32 v[6:7], v[50:51], v[50:51]
	v_pk_add_f32 v[4:5], v[4:5], v[4:5] op_sel_hi:[0,1]
	v_mov_b32_e32 v81, v7
	v_pk_mov_b32 v[6:7], v[142:143], v[6:7] op_sel:[1,0]
	v_pk_fma_f32 v[82:83], v[42:43], v[42:43], v[138:139] op_sel_hi:[1,1,0]
	v_pk_add_f32 v[6:7], v[6:7], v[80:81]
	v_pk_fma_f32 v[80:81], v[40:41], v[40:41], v[140:141] op_sel_hi:[1,1,0]
	v_pk_add_f32 v[6:7], v[6:7], v[6:7] op_sel_hi:[0,1]
	v_mov_b32_e32 v129, v81
	v_mov_b32_e32 v133, v83
	v_mov_b32_e32 v125, v7
	v_mov_b32_e32 v127, v5
	v_pk_add_f32 v[80:81], v[128:129], v[132:133]
	v_pk_add_f32 v[4:5], v[124:125], v[126:127]
	v_pk_mul_f32 v[6:7], v[26:27], v[26:27]
	v_pk_add_f32 v[4:5], v[80:81], v[4:5]
	v_mov_b32_e32 v80, v136
	v_mov_b32_e32 v81, v7
	v_pk_mov_b32 v[6:7], v[136:137], v[6:7] op_sel:[1,0]
	s_add_u32 s44, s12, s44
	v_pk_add_f32 v[6:7], v[6:7], v[80:81]
	s_addc_u32 s45, s15, s45
	v_pk_add_f32 v[4:5], v[4:5], v[4:5] op_sel_hi:[0,1]
	v_pk_add_f32 v[6:7], v[6:7], v[6:7] op_sel_hi:[0,1]
	v_pk_fma_f32 v[80:81], v[16:17], v[16:17], v[134:135] op_sel_hi:[1,1,0]
	v_pk_fma_f32 v[82:83], v[18:19], v[18:19], v[130:131] op_sel_hi:[1,1,0]
	s_add_u32 s0, s12, s46
	v_mov_b32_e32 v121, v81
	v_mov_b32_e32 v123, v83
	v_mov_b32_e32 v117, v7
	v_mov_b32_e32 v119, v5
	s_addc_u32 s1, s15, s47
	v_pk_add_f32 v[80:81], v[120:121], v[122:123]
	v_pk_add_f32 v[4:5], v[116:117], v[118:119]
	s_add_u32 s36, s2, 0x2000
	v_pk_add_f32 v[120:121], v[80:81], v[4:5]
	v_and_b32_e32 v5, 64, v207
	s_addc_u32 s37, s3, 0
	v_xor_b32_e32 v4, 16, v207
	v_add_u32_e32 v130, 64, v5
	s_add_u32 s46, s44, 0x2000
	v_cmp_lt_i32_e32 vcc, v4, v130
	s_addc_u32 s47, s45, 0
	v_mov_b32_e32 v124, v61
	v_cndmask_b32_e32 v4, v207, v4, vcc
	v_lshlrev_b32_e32 v131, 2, v4
	global_load_dwordx4 v[144:147], v2, s[46:47]
	global_load_dwordx4 v[148:151], v2, s[36:37]
	global_load_dwordx4 v[152:155], v2, s[44:45]
	global_load_dwordx4 v[164:167], v156, s[36:37]
	global_load_dwordx4 v[168:171], v156, s[46:47]
	global_load_dwordx4 v[172:175], v2, s[44:45] offset:1024
	global_load_dwordx4 v[176:179], v157, s[36:37]
	global_load_dwordx4 v[180:183], v157, s[46:47]
	global_load_dwordx4 v[184:187], v2, s[44:45] offset:2048
	global_load_dwordx4 v[190:193], v158, s[36:37]
	global_load_dwordx4 v[212:215], v158, s[46:47]
	global_load_dwordx4 v[216:219], v2, s[44:45] offset:3072
	global_load_dwordx4 v[224:227], v159, s[36:37]
	global_load_dwordx4 v[228:231], v159, s[46:47]
	global_load_dwordx4 v[232:235], v159, s[44:45]
	global_load_dwordx4 v[236:239], v160, s[36:37]
	global_load_dwordx4 v[240:243], v160, s[46:47]
	global_load_dwordx4 v[244:247], v160, s[44:45]
	global_load_dwordx4 v[248:251], v161, s[36:37]
	v_mov_b32_e32 v125, v53
	v_mov_b32_e32 v128, v63
	v_mov_b32_e32 v129, v55
	v_mov_b32_e32 v122, v60
	v_mov_b32_e32 v123, v52
	v_pk_mul_f32 v[124:125], v[124:125], v[124:125]
	v_mov_b32_e32 v126, v62
	v_mov_b32_e32 v127, v54
	v_pk_mul_f32 v[128:129], v[128:129], v[128:129]
	v_pk_fma_f32 v[122:123], v[122:123], v[122:123], v[124:125]
	v_pk_fma_f32 v[124:125], v[126:127], v[126:127], v[128:129]
	v_mov_b32_e32 v126, v114
	v_pk_add_f32 v[122:123], v[122:123], v[124:125]
	v_pk_mul_f32 v[124:125], v[46:47], v[46:47]
	v_pk_add_f32 v[122:123], v[122:123], v[122:123] op_sel_hi:[0,1]
	v_mov_b32_e32 v127, v125
	v_pk_mov_b32 v[114:115], v[114:115], v[124:125] op_sel:[1,0]
	v_pk_fma_f32 v[112:113], v[36:37], v[36:37], v[112:113] op_sel_hi:[1,1,0]
	v_pk_add_f32 v[114:115], v[114:115], v[126:127]
	v_pk_fma_f32 v[110:111], v[38:39], v[38:39], v[110:111] op_sel_hi:[1,1,0]
	v_pk_add_f32 v[114:115], v[114:115], v[114:115] op_sel_hi:[0,1]
	v_mov_b32_e32 v105, v113
	v_mov_b32_e32 v107, v111
	v_mov_b32_e32 v97, v115
	v_mov_b32_e32 v99, v123
	v_pk_add_f32 v[104:105], v[104:105], v[106:107]
	v_pk_add_f32 v[96:97], v[96:97], v[98:99]
	v_pk_mul_f32 v[98:99], v[22:23], v[22:23]
	v_pk_add_f32 v[96:97], v[104:105], v[96:97]
	v_mov_b32_e32 v104, v108
	v_mov_b32_e32 v105, v99
	v_pk_mov_b32 v[98:99], v[108:109], v[98:99] op_sel:[1,0]
	v_pk_add_f32 v[96:97], v[96:97], v[96:97] op_sel_hi:[0,1]
	v_pk_add_f32 v[98:99], v[98:99], v[104:105]
	v_pk_fma_f32 v[102:103], v[12:13], v[12:13], v[102:103] op_sel_hi:[1,1,0]
	v_pk_add_f32 v[98:99], v[98:99], v[98:99] op_sel_hi:[0,1]
	v_pk_fma_f32 v[100:101], v[14:15], v[14:15], v[100:101] op_sel_hi:[1,1,0]
	v_mov_b32_e32 v93, v103
	v_mov_b32_e32 v95, v101
	v_mov_b32_e32 v89, v99
	v_mov_b32_e32 v91, v97
	v_pk_add_f32 v[92:93], v[92:93], v[94:95]
	v_pk_add_f32 v[88:89], v[88:89], v[90:91]
	v_mov_b32_e32 v91, v120
	v_pk_add_f32 v[88:89], v[92:93], v[88:89]
	v_xor_b32_e32 v92, 32, v207
	v_mov_b32_e32 v90, v88
	v_mov_b32_e32 v120, v89
	v_pk_add_f32 v[88:89], v[90:91], v[120:121]
	v_cmp_lt_i32_e32 vcc, v92, v130
	s_mov_b32 s2, 0x3a000000
	v_mov_b32_dpp v91, v89 quad_perm:[1,0,3,2] row_mask:0xf bank_mask:0xf bound_ctrl:1
	v_mov_b32_dpp v90, v88 quad_perm:[1,0,3,2] row_mask:0xf bank_mask:0xf bound_ctrl:1
	v_pk_add_f32 v[88:89], v[88:89], v[90:91]
	v_cndmask_b32_e32 v92, v207, v92, vcc
	v_lshlrev_b32_e32 v92, 2, v92
	v_mov_b32_dpp v91, v89 quad_perm:[2,3,0,1] row_mask:0xf bank_mask:0xf bound_ctrl:1
	v_mov_b32_dpp v90, v88 quad_perm:[2,3,0,1] row_mask:0xf bank_mask:0xf bound_ctrl:1
	v_pk_add_f32 v[88:89], v[88:89], v[90:91]
	s_waitcnt vmcnt(18)
	v_mov_b32_e32 v4, v144
	v_mov_b32_e32 v5, v145
	v_mov_b32_e32 v6, v146
	v_mov_b32_e32 v7, v147
	global_load_dwordx4 v[144:147], v161, s[46:47]
	v_pk_add_f32 v[6:7], v[6:7], 1.0 op_sel_hi:[1,0]
	v_mov_b32_dpp v91, v89 row_half_mirror row_mask:0xf bank_mask:0xf bound_ctrl:1
	v_mov_b32_dpp v90, v88 row_half_mirror row_mask:0xf bank_mask:0xf bound_ctrl:1
	v_pk_add_f32 v[88:89], v[88:89], v[90:91]
	v_pk_add_f32 v[4:5], v[4:5], 1.0 op_sel_hi:[1,0]
	s_nop 0
	v_mov_b32_dpp v91, v89 row_mirror row_mask:0xf bank_mask:0xf bound_ctrl:1
	v_mov_b32_dpp v90, v88 row_mirror row_mask:0xf bank_mask:0xf bound_ctrl:1
	v_pk_add_f32 v[88:89], v[88:89], v[90:91]
	ds_bpermute_b32 v91, v131, v89
	ds_bpermute_b32 v90, v131, v88
	s_waitcnt lgkmcnt(0)
	v_pk_add_f32 v[88:89], v[88:89], v[90:91]
	ds_bpermute_b32 v91, v92, v89
	ds_bpermute_b32 v90, v92, v88
	s_waitcnt lgkmcnt(0)
	v_pk_add_f32 v[88:89], v[88:89], v[90:91]
	s_nop 0
	v_pk_fma_f32 v[88:89], v[88:89], s[2:3], v[188:189] op_sel_hi:[1,0,0]
	s_nop 0
	v_mul_f32_e32 v90, 0x4b800000, v89
	v_cmp_gt_f32_e32 vcc, s11, v89
	s_nop 1
	v_cndmask_b32_e32 v89, v89, v90, vcc
	v_rsq_f32_e32 v89, v89
	v_lshl_add_u64 v[90:91], s[42:43], 1, v[78:79]
	s_add_u32 s42, s0, 0x2000
	s_addc_u32 s43, s1, 0
	v_mul_f32_e32 v92, 0x45800000, v89
	v_cndmask_b32_e32 v92, v89, v92, vcc
	v_pk_mul_f32 v[66:67], v[66:67], v[92:93] op_sel_hi:[1,0]
	v_pk_mul_f32 v[64:65], v[64:65], v[92:93] op_sel_hi:[1,0]
	s_waitcnt vmcnt(18)
	v_mov_b32_e32 v80, v148
	v_mov_b32_e32 v81, v149
	v_mov_b32_e32 v82, v150
	v_mov_b32_e32 v83, v151
	global_load_dwordx4 v[148:151], v161, s[44:45]
	v_pk_mul_f32 v[66:67], v[82:83], v[66:67]
	v_pk_mul_f32 v[64:65], v[80:81], v[64:65]
	s_waitcnt vmcnt(18)
	v_mov_b32_e32 v116, v152
	v_mov_b32_e32 v117, v153
	v_mov_b32_e32 v118, v154
	v_mov_b32_e32 v119, v155
	global_load_dwordx4 v[152:155], v162, s[36:37]
	v_pk_fma_f32 v[6:7], v[6:7], v[66:67], v[118:119]
	v_pk_fma_f32 v[4:5], v[4:5], v[64:65], v[116:117]
	v_pk_mul_f32 v[58:59], v[58:59], v[92:93] op_sel_hi:[1,0]
	v_cvt_pk_bf16_f32 v4, v4, v5
	v_cvt_pk_bf16_f32 v5, v6, v7
	global_store_dwordx2 v[90:91], v[4:5], off
	s_nop 0
	v_pk_mul_f32 v[56:57], v[56:57], v[92:93] op_sel_hi:[1,0]
	v_pk_mul_f32 v[50:51], v[50:51], v[92:93] op_sel_hi:[1,0]
	v_pk_mul_f32 v[48:49], v[48:49], v[92:93] op_sel_hi:[1,0]
	v_pk_mul_f32 v[42:43], v[42:43], v[92:93] op_sel_hi:[1,0]
	v_pk_mul_f32 v[40:41], v[40:41], v[92:93] op_sel_hi:[1,0]
	v_pk_mul_f32 v[34:35], v[34:35], v[92:93] op_sel_hi:[1,0]
	v_pk_mul_f32 v[32:33], v[32:33], v[92:93] op_sel_hi:[1,0]
	v_pk_mul_f32 v[26:27], v[26:27], v[92:93] op_sel_hi:[1,0]
	v_pk_mul_f32 v[24:25], v[24:25], v[92:93] op_sel_hi:[1,0]
	v_pk_mul_f32 v[18:19], v[18:19], v[92:93] op_sel_hi:[1,0]
	v_pk_mul_f32 v[16:17], v[16:17], v[92:93] op_sel_hi:[1,0]
	v_cmp_gt_f32_e32 vcc, s11, v88
	s_waitcnt vmcnt(19)
	v_mov_b32_e32 v4, v164
	v_mov_b32_e32 v5, v165
	v_mov_b32_e32 v6, v166
	v_mov_b32_e32 v7, v167
	global_load_dwordx4 v[164:167], v162, s[46:47]
	v_pk_mul_f32 v[4:5], v[4:5], v[56:57]
	v_pk_mul_f32 v[6:7], v[6:7], v[58:59]
	s_waitcnt vmcnt(19)
	v_mov_b32_e32 v64, v168
	v_mov_b32_e32 v65, v169
	v_mov_b32_e32 v66, v170
	v_mov_b32_e32 v67, v171
	global_load_dwordx4 v[168:171], v162, s[44:45]
	v_pk_add_f32 v[56:57], v[66:67], 1.0 op_sel_hi:[1,0]
	v_pk_add_f32 v[58:59], v[64:65], 1.0 op_sel_hi:[1,0]
	s_waitcnt vmcnt(19)
	v_mov_b32_e32 v80, v172
	v_mov_b32_e32 v81, v173
	v_mov_b32_e32 v82, v174
	v_mov_b32_e32 v83, v175
	global_load_dwordx4 v[172:175], v2, s[36:37]
	v_pk_fma_f32 v[6:7], v[56:57], v[6:7], v[82:83]
	v_pk_fma_f32 v[4:5], v[58:59], v[4:5], v[80:81]
	s_nop 0
	v_cvt_pk_bf16_f32 v4, v4, v5
	v_cvt_pk_bf16_f32 v5, v6, v7
	global_store_dwordx2 v[90:91], v[4:5], off offset:512
	s_nop 0
	s_waitcnt vmcnt(20)
	v_mov_b32_e32 v4, v176
	v_mov_b32_e32 v5, v177
	v_mov_b32_e32 v6, v178
	v_mov_b32_e32 v7, v179
	global_load_dwordx4 v[176:179], v2, s[42:43]
	v_pk_mul_f32 v[4:5], v[4:5], v[48:49]
	v_pk_mul_f32 v[6:7], v[6:7], v[50:51]
	s_waitcnt vmcnt(20)
	v_mov_b32_e32 v56, v180
	v_mov_b32_e32 v57, v181
	v_mov_b32_e32 v58, v182
	v_mov_b32_e32 v59, v183
	global_load_dwordx4 v[180:183], v2, s[0:1]
	v_pk_add_f32 v[48:49], v[58:59], 1.0 op_sel_hi:[1,0]
	v_pk_add_f32 v[50:51], v[56:57], 1.0 op_sel_hi:[1,0]
	s_waitcnt vmcnt(20)
	v_mov_b32_e32 v64, v184
	v_mov_b32_e32 v65, v185
	v_mov_b32_e32 v66, v186
	v_mov_b32_e32 v67, v187
	global_load_dwordx4 v[184:187], v156, s[36:37]
	v_pk_fma_f32 v[6:7], v[48:49], v[6:7], v[66:67]
	v_pk_fma_f32 v[4:5], v[50:51], v[4:5], v[64:65]
	s_nop 0
	v_cvt_pk_bf16_f32 v4, v4, v5
	v_cvt_pk_bf16_f32 v5, v6, v7
	global_store_dwordx2 v[90:91], v[4:5], off offset:1024
	s_nop 0
	s_waitcnt vmcnt(21)
	v_mov_b32_e32 v4, v190
	v_mov_b32_e32 v5, v191
	v_mov_b32_e32 v6, v192
	v_mov_b32_e32 v7, v193
	global_load_dwordx4 v[190:193], v156, s[42:43]
	v_pk_mul_f32 v[4:5], v[40:41], v[4:5]
	v_pk_mul_f32 v[6:7], v[42:43], v[6:7]
	s_waitcnt vmcnt(21)
	v_mov_b32_e32 v48, v212
	v_mov_b32_e32 v49, v213
	v_mov_b32_e32 v50, v214
	v_mov_b32_e32 v51, v215
	global_load_dwordx4 v[212:215], v2, s[0:1] offset:1024
	v_pk_add_f32 v[40:41], v[50:51], 1.0 op_sel_hi:[1,0]
	v_pk_add_f32 v[42:43], v[48:49], 1.0 op_sel_hi:[1,0]
	s_waitcnt vmcnt(21)
	v_mov_b32_e32 v56, v216
	v_mov_b32_e32 v57, v217
	v_mov_b32_e32 v58, v218
	v_mov_b32_e32 v59, v219
	global_load_dwordx4 v[216:219], v157, s[36:37]
	v_pk_fma_f32 v[6:7], v[6:7], v[40:41], v[58:59]
	v_pk_fma_f32 v[4:5], v[4:5], v[42:43], v[56:57]
	s_nop 0
	v_cvt_pk_bf16_f32 v4, v4, v5
	v_cvt_pk_bf16_f32 v5, v6, v7
	global_store_dwordx2 v[90:91], v[4:5], off offset:1536
	s_nop 0
	s_waitcnt vmcnt(22)
	v_mov_b32_e32 v4, v224
	v_mov_b32_e32 v5, v225
	v_mov_b32_e32 v6, v226
	v_mov_b32_e32 v7, v227
	global_load_dwordx4 v[224:227], v157, s[42:43]
	v_pk_mul_f32 v[4:5], v[32:33], v[4:5]
	v_pk_mul_f32 v[6:7], v[34:35], v[6:7]
	s_waitcnt vmcnt(22)
	v_mov_b32_e32 v40, v228
	v_mov_b32_e32 v41, v229
	v_mov_b32_e32 v42, v230
	v_mov_b32_e32 v43, v231
	global_load_dwordx4 v[228:231], v2, s[0:1] offset:2048
	v_pk_add_f32 v[32:33], v[42:43], 1.0 op_sel_hi:[1,0]
	v_pk_add_f32 v[34:35], v[40:41], 1.0 op_sel_hi:[1,0]
	s_waitcnt vmcnt(22)
	v_mov_b32_e32 v48, v232
	v_mov_b32_e32 v49, v233
	v_mov_b32_e32 v50, v234
	v_mov_b32_e32 v51, v235
	global_load_dwordx4 v[232:235], v158, s[36:37]
	v_pk_fma_f32 v[6:7], v[6:7], v[32:33], v[50:51]
	v_pk_fma_f32 v[4:5], v[4:5], v[34:35], v[48:49]
	s_nop 0
	v_cvt_pk_bf16_f32 v4, v4, v5
	v_cvt_pk_bf16_f32 v5, v6, v7
	global_store_dwordx2 v[90:91], v[4:5], off offset:2048
	s_nop 0
	s_waitcnt vmcnt(23)
	v_mov_b32_e32 v4, v236
	v_mov_b32_e32 v5, v237
	v_mov_b32_e32 v6, v238
	v_mov_b32_e32 v7, v239
	global_load_dwordx4 v[236:239], v158, s[42:43]
	v_pk_mul_f32 v[4:5], v[24:25], v[4:5]
	v_pk_mul_f32 v[6:7], v[26:27], v[6:7]
	s_waitcnt vmcnt(23)
	v_mov_b32_e32 v32, v240
	v_mov_b32_e32 v33, v241
	v_mov_b32_e32 v34, v242
	v_mov_b32_e32 v35, v243
	global_load_dwordx4 v[240:243], v2, s[0:1] offset:3072
	v_pk_add_f32 v[24:25], v[34:35], 1.0 op_sel_hi:[1,0]
	v_pk_add_f32 v[26:27], v[32:33], 1.0 op_sel_hi:[1,0]
	s_waitcnt vmcnt(23)
	v_mov_b32_e32 v40, v244
	v_mov_b32_e32 v41, v245
	v_mov_b32_e32 v42, v246
	v_mov_b32_e32 v43, v247
	global_load_dwordx4 v[244:247], v159, s[36:37]
	v_pk_fma_f32 v[6:7], v[6:7], v[24:25], v[42:43]
	v_pk_fma_f32 v[4:5], v[4:5], v[26:27], v[40:41]
	s_nop 0
	v_cvt_pk_bf16_f32 v4, v4, v5
	v_cvt_pk_bf16_f32 v5, v6, v7
	global_store_dwordx2 v[90:91], v[4:5], off offset:2560
	s_nop 0
	s_waitcnt vmcnt(24)
	v_mov_b32_e32 v4, v248
	v_mov_b32_e32 v5, v249
	v_mov_b32_e32 v6, v250
	v_mov_b32_e32 v7, v251
	global_load_dwordx4 v[248:251], v159, s[42:43]
	v_pk_mul_f32 v[4:5], v[16:17], v[4:5]
	v_pk_mul_f32 v[6:7], v[18:19], v[6:7]
	s_waitcnt vmcnt(24)
	v_mov_b32_e32 v24, v144
	v_mov_b32_e32 v25, v145
	v_mov_b32_e32 v26, v146
	v_mov_b32_e32 v27, v147
	global_load_dwordx4 v[144:147], v159, s[0:1]
	v_pk_add_f32 v[16:17], v[26:27], 1.0 op_sel_hi:[1,0]
	v_pk_add_f32 v[18:19], v[24:25], 1.0 op_sel_hi:[1,0]
	s_waitcnt vmcnt(24)
	v_mov_b32_e32 v32, v148
	v_mov_b32_e32 v33, v149
	v_mov_b32_e32 v34, v150
	v_mov_b32_e32 v35, v151
	global_load_dwordx4 v[148:151], v160, s[36:37]
	v_pk_fma_f32 v[6:7], v[6:7], v[16:17], v[34:35]
	v_pk_fma_f32 v[4:5], v[4:5], v[18:19], v[32:33]
	v_pk_mul_f32 v[32:33], v[84:85], v[92:93] op_sel_hi:[1,0]
	v_cvt_pk_bf16_f32 v4, v4, v5
	v_cvt_pk_bf16_f32 v5, v6, v7
	global_store_dwordx2 v[90:91], v[4:5], off offset:3072
	s_nop 0
	v_pk_mul_f32 v[34:35], v[86:87], v[92:93] op_sel_hi:[1,0]
	s_waitcnt vmcnt(25)
	v_mov_b32_e32 v4, v152
	v_mov_b32_e32 v5, v153
	v_mov_b32_e32 v6, v154
	v_mov_b32_e32 v7, v155
	global_load_dwordx4 v[152:155], v160, s[42:43]
	v_pk_mul_f32 v[6:7], v[32:33], v[6:7]
	v_pk_mul_f32 v[4:5], v[34:35], v[4:5]
	s_waitcnt vmcnt(24)
	v_mov_b32_e32 v16, v164
	v_mov_b32_e32 v17, v165
	v_mov_b32_e32 v18, v166
	v_mov_b32_e32 v19, v167
	global_load_dwordx4 v[164:167], v160, s[0:1]
	v_pk_add_f32 v[18:19], v[18:19], 1.0 op_sel_hi:[1,0]
	v_pk_add_f32 v[16:17], v[16:17], 1.0 op_sel_hi:[1,0]
	s_waitcnt vmcnt(24)
	v_mov_b32_e32 v24, v168
	v_mov_b32_e32 v25, v169
	v_mov_b32_e32 v26, v170
	v_mov_b32_e32 v27, v171
	global_load_dwordx4 v[168:171], v161, s[36:37]
	v_pk_fma_f32 v[6:7], v[6:7], v[18:19], v[26:27]
	v_pk_fma_f32 v[4:5], v[4:5], v[16:17], v[24:25]
	v_mul_f32_e32 v32, 0x4b800000, v88
	v_cvt_pk_bf16_f32 v4, v4, v5
	v_cvt_pk_bf16_f32 v5, v6, v7
	global_store_dwordx2 v[90:91], v[4:5], off offset:3584
	s_nop 0
	v_cndmask_b32_e32 v32, v88, v32, vcc
	v_rsq_f32_e32 v34, v32
	v_lshl_add_u64 v[32:33], s[40:41], 1, v[78:79]
	v_mul_f32_e32 v35, 0x45800000, v34
	v_cndmask_b32_e32 v34, v34, v35, vcc
	v_pk_mul_f32 v[40:41], v[62:63], v[34:35] op_sel_hi:[1,0]
	v_pk_mul_f32 v[42:43], v[60:61], v[34:35] op_sel_hi:[1,0]
	v_pk_mul_f32 v[38:39], v[38:39], v[34:35] op_sel_hi:[1,0]
	v_pk_mul_f32 v[36:37], v[36:37], v[34:35] op_sel_hi:[1,0]
	v_pk_mul_f32 v[30:31], v[30:31], v[34:35] op_sel_hi:[1,0]
	v_pk_mul_f32 v[28:29], v[28:29], v[34:35] op_sel_hi:[1,0]
	v_pk_mul_f32 v[22:23], v[22:23], v[34:35] op_sel_hi:[1,0]
	v_pk_mul_f32 v[20:21], v[20:21], v[34:35] op_sel_hi:[1,0]
	v_pk_mul_f32 v[14:15], v[14:15], v[34:35] op_sel_hi:[1,0]
	v_pk_mul_f32 v[12:13], v[12:13], v[34:35] op_sel_hi:[1,0]
	v_pk_mul_f32 v[10:11], v[10:11], v[34:35] op_sel_hi:[1,0]
	v_pk_mul_f32 v[8:9], v[8:9], v[34:35] op_sel_hi:[1,0]
	s_waitcnt vmcnt(25)
	v_mov_b32_e32 v4, v172
	v_mov_b32_e32 v5, v173
	v_mov_b32_e32 v6, v174
	v_mov_b32_e32 v7, v175
	global_load_dwordx4 v[172:175], v161, s[42:43]
	v_pk_mul_f32 v[4:5], v[4:5], v[42:43]
	v_pk_mul_f32 v[6:7], v[6:7], v[40:41]
	s_waitcnt vmcnt(24)
	v_mov_b32_e32 v16, v176
	v_mov_b32_e32 v17, v177
	v_mov_b32_e32 v18, v178
	v_mov_b32_e32 v19, v179
	global_load_dwordx4 v[176:179], v161, s[0:1]
	v_pk_add_f32 v[18:19], v[18:19], 1.0 op_sel_hi:[1,0]
	v_pk_add_f32 v[16:17], v[16:17], 1.0 op_sel_hi:[1,0]
	s_waitcnt vmcnt(24)
	v_mov_b32_e32 v24, v180
	v_mov_b32_e32 v25, v181
	v_mov_b32_e32 v26, v182
	v_mov_b32_e32 v27, v183
	global_load_dwordx4 v[180:183], v162, s[36:37]
	v_pk_fma_f32 v[6:7], v[18:19], v[6:7], v[26:27]
	v_pk_fma_f32 v[4:5], v[16:17], v[4:5], v[24:25]
	v_pk_mul_f32 v[40:41], v[54:55], v[34:35] op_sel_hi:[1,0]
	v_cvt_pk_bf16_f32 v4, v4, v5
	v_cvt_pk_bf16_f32 v5, v6, v7
	global_store_dwordx2 v[32:33], v[4:5], off
	s_nop 0
	v_pk_mul_f32 v[42:43], v[52:53], v[34:35] op_sel_hi:[1,0]
	s_waitcnt vmcnt(25)
	v_mov_b32_e32 v4, v184
	v_mov_b32_e32 v5, v185
	v_mov_b32_e32 v6, v186
	v_mov_b32_e32 v7, v187
	global_load_dwordx4 v[184:187], v162, s[42:43]
	v_pk_mul_f32 v[6:7], v[6:7], v[40:41]
	v_pk_mul_f32 v[4:5], v[4:5], v[42:43]
	s_waitcnt vmcnt(24)
	v_mov_b32_e32 v16, v190
	v_mov_b32_e32 v17, v191
	v_mov_b32_e32 v18, v192
	v_mov_b32_e32 v19, v193
	global_load_dwordx4 v[190:193], v162, s[0:1]
	v_pk_add_f32 v[18:19], v[18:19], 1.0 op_sel_hi:[1,0]
	v_pk_add_f32 v[16:17], v[16:17], 1.0 op_sel_hi:[1,0]
	s_waitcnt vmcnt(24)
	v_mov_b32_e32 v24, v212
	v_mov_b32_e32 v25, v213
	v_mov_b32_e32 v26, v214
	v_mov_b32_e32 v27, v215
	v_pk_fma_f32 v[6:7], v[18:19], v[6:7], v[26:27]
	v_pk_fma_f32 v[4:5], v[16:17], v[4:5], v[24:25]
	v_pk_mul_f32 v[40:41], v[46:47], v[34:35] op_sel_hi:[1,0]
	v_cvt_pk_bf16_f32 v4, v4, v5
	v_cvt_pk_bf16_f32 v5, v6, v7
	global_store_dwordx2 v[32:33], v[4:5], off offset:512
	s_nop 0
	v_pk_mul_f32 v[42:43], v[44:45], v[34:35] op_sel_hi:[1,0]
	s_waitcnt vmcnt(24)
	v_mov_b32_e32 v4, v216
	v_mov_b32_e32 v5, v217
	v_mov_b32_e32 v6, v218
	v_mov_b32_e32 v7, v219
	v_pk_mul_f32 v[6:7], v[6:7], v[40:41]
	v_pk_mul_f32 v[4:5], v[4:5], v[42:43]
	s_waitcnt vmcnt(22)
	v_mov_b32_e32 v16, v224
	v_mov_b32_e32 v17, v225
	v_mov_b32_e32 v18, v226
	v_mov_b32_e32 v19, v227
	v_pk_add_f32 v[18:19], v[18:19], 1.0 op_sel_hi:[1,0]
	v_pk_add_f32 v[16:17], v[16:17], 1.0 op_sel_hi:[1,0]
	s_waitcnt vmcnt(21)
	v_mov_b32_e32 v24, v228
	v_mov_b32_e32 v25, v229
	v_mov_b32_e32 v26, v230
	v_mov_b32_e32 v27, v231
	v_pk_fma_f32 v[6:7], v[18:19], v[6:7], v[26:27]
	v_pk_fma_f32 v[4:5], v[16:17], v[4:5], v[24:25]
	s_nop 0
	v_cvt_pk_bf16_f32 v4, v4, v5
	v_cvt_pk_bf16_f32 v5, v6, v7
	global_store_dwordx2 v[32:33], v[4:5], off offset:1024
	s_nop 0
	s_waitcnt vmcnt(21)
	v_mov_b32_e32 v4, v232
	v_mov_b32_e32 v5, v233
	v_mov_b32_e32 v6, v234
	v_mov_b32_e32 v7, v235
	v_pk_mul_f32 v[4:5], v[4:5], v[36:37]
	v_pk_mul_f32 v[6:7], v[6:7], v[38:39]
	s_waitcnt vmcnt(19)
	v_mov_b32_e32 v16, v236
	v_mov_b32_e32 v17, v237
	v_mov_b32_e32 v18, v238
	v_mov_b32_e32 v19, v239
	v_pk_add_f32 v[18:19], v[18:19], 1.0 op_sel_hi:[1,0]
	v_pk_add_f32 v[16:17], v[16:17], 1.0 op_sel_hi:[1,0]
	s_waitcnt vmcnt(18)
	v_mov_b32_e32 v24, v240
	v_mov_b32_e32 v25, v241
	v_mov_b32_e32 v26, v242
	v_mov_b32_e32 v27, v243
	v_pk_fma_f32 v[6:7], v[6:7], v[18:19], v[26:27]
	v_pk_fma_f32 v[4:5], v[4:5], v[16:17], v[24:25]
	s_nop 0
	v_cvt_pk_bf16_f32 v4, v4, v5
	v_cvt_pk_bf16_f32 v5, v6, v7
	global_store_dwordx2 v[32:33], v[4:5], off offset:1536
	s_nop 0
	s_waitcnt vmcnt(18)
	v_mov_b32_e32 v4, v244
	v_mov_b32_e32 v5, v245
	v_mov_b32_e32 v6, v246
	v_mov_b32_e32 v7, v247
	v_pk_mul_f32 v[4:5], v[28:29], v[4:5]
	v_pk_mul_f32 v[6:7], v[30:31], v[6:7]
	s_waitcnt vmcnt(16)
	v_mov_b32_e32 v16, v248
	v_mov_b32_e32 v17, v249
	v_mov_b32_e32 v18, v250
	v_mov_b32_e32 v19, v251
	v_pk_add_f32 v[18:19], v[18:19], 1.0 op_sel_hi:[1,0]
	v_pk_add_f32 v[16:17], v[16:17], 1.0 op_sel_hi:[1,0]
	s_waitcnt vmcnt(15)
	v_mov_b32_e32 v24, v144
	v_mov_b32_e32 v25, v145
	v_mov_b32_e32 v26, v146
	v_mov_b32_e32 v27, v147
	v_pk_fma_f32 v[6:7], v[6:7], v[18:19], v[26:27]
	v_pk_fma_f32 v[4:5], v[4:5], v[16:17], v[24:25]
	s_nop 0
	v_cvt_pk_bf16_f32 v4, v4, v5
	v_cvt_pk_bf16_f32 v5, v6, v7
	global_store_dwordx2 v[32:33], v[4:5], off offset:2048
	s_nop 0
	s_waitcnt vmcnt(15)
	v_mov_b32_e32 v4, v148
	v_mov_b32_e32 v5, v149
	v_mov_b32_e32 v6, v150
	v_mov_b32_e32 v7, v151
	v_pk_mul_f32 v[4:5], v[20:21], v[4:5]
	v_pk_mul_f32 v[6:7], v[22:23], v[6:7]
	s_waitcnt vmcnt(13)
	v_mov_b32_e32 v16, v152
	v_mov_b32_e32 v17, v153
	v_mov_b32_e32 v18, v154
	v_mov_b32_e32 v19, v155
	v_pk_add_f32 v[18:19], v[18:19], 1.0 op_sel_hi:[1,0]
	v_pk_add_f32 v[16:17], v[16:17], 1.0 op_sel_hi:[1,0]
	s_waitcnt vmcnt(12)
	v_mov_b32_e32 v24, v164
	v_mov_b32_e32 v25, v165
	v_mov_b32_e32 v26, v166
	v_mov_b32_e32 v27, v167
	v_pk_fma_f32 v[6:7], v[6:7], v[18:19], v[26:27]
	v_pk_fma_f32 v[4:5], v[4:5], v[16:17], v[24:25]
	s_nop 0
	v_cvt_pk_bf16_f32 v4, v4, v5
	v_cvt_pk_bf16_f32 v5, v6, v7
	global_store_dwordx2 v[32:33], v[4:5], off offset:2560
	s_nop 0
	s_waitcnt vmcnt(12)
	v_mov_b32_e32 v4, v168
	v_mov_b32_e32 v5, v169
	v_mov_b32_e32 v6, v170
	v_mov_b32_e32 v7, v171
	v_pk_mul_f32 v[4:5], v[12:13], v[4:5]
	v_pk_mul_f32 v[6:7], v[14:15], v[6:7]
	s_waitcnt vmcnt(10)
	v_mov_b32_e32 v16, v172
	v_mov_b32_e32 v17, v173
	v_mov_b32_e32 v18, v174
	v_mov_b32_e32 v19, v175
	v_pk_add_f32 v[12:13], v[18:19], 1.0 op_sel_hi:[1,0]
	v_pk_add_f32 v[14:15], v[16:17], 1.0 op_sel_hi:[1,0]
	s_waitcnt vmcnt(9)
	v_mov_b32_e32 v20, v176
	v_mov_b32_e32 v21, v177
	v_mov_b32_e32 v22, v178
	v_mov_b32_e32 v23, v179
	v_pk_fma_f32 v[6:7], v[6:7], v[12:13], v[22:23]
	v_pk_fma_f32 v[4:5], v[4:5], v[14:15], v[20:21]
	s_nop 0
	v_cvt_pk_bf16_f32 v4, v4, v5
	v_cvt_pk_bf16_f32 v5, v6, v7
	global_store_dwordx2 v[32:33], v[4:5], off offset:3072
	s_nop 0
	s_waitcnt vmcnt(9)
	v_mov_b32_e32 v4, v180
	v_mov_b32_e32 v5, v181
	v_mov_b32_e32 v6, v182
	v_mov_b32_e32 v7, v183
	v_pk_mul_f32 v[4:5], v[8:9], v[4:5]
	v_pk_mul_f32 v[6:7], v[10:11], v[6:7]
	s_waitcnt vmcnt(7)
	v_mov_b32_e32 v12, v184
	v_mov_b32_e32 v13, v185
	v_mov_b32_e32 v14, v186
	v_mov_b32_e32 v15, v187
	v_pk_add_f32 v[8:9], v[14:15], 1.0 op_sel_hi:[1,0]
	v_pk_add_f32 v[10:11], v[12:13], 1.0 op_sel_hi:[1,0]
	s_waitcnt vmcnt(6)
	v_mov_b32_e32 v16, v190
	v_mov_b32_e32 v17, v191
	v_mov_b32_e32 v18, v192
	v_mov_b32_e32 v19, v193
	v_pk_fma_f32 v[6:7], v[6:7], v[8:9], v[18:19]
	v_pk_fma_f32 v[4:5], v[4:5], v[10:11], v[16:17]
	s_nop 0
	v_cvt_pk_bf16_f32 v4, v4, v5
	v_cvt_pk_bf16_f32 v5, v6, v7
	global_store_dwordx2 v[32:33], v[4:5], off offset:3584
